# stack: attention LDS-read prefetch reschedule, conflict-free MLA K-tile swizzle, unscaled fp8 MFMA form (unit scales)
# speedup vs baseline: 1.0059x; 1.0059x over previous
; __device__ __forceinline__ int v_st(int k, int c) { const int kk = (k & ~0xC) | ((k & 4) << 1) | ((k & 8) >> 1); return ((kk >> 3) * 4 + (c >> 5)) * 512 + ((kk & 7) * 32 + (c & 31)) * 2; }
; __device__ __forceinline__ int v_rd_base(int lane) { return ((lane & 3) << 3) | (((lane >> 2) & 3) << 6) | (((lane >> 4) & 1) << 5) | (((lane >> 5) & 1) << 8); }
; template <int DQK, int KB>
; __device__ __forceinline__ void qkt(f32x16& p0, f32x16& p1, const char* K_lds, int r32, int hi, const bf16x8* qr) {
;     ...
;     const char* kb[4];
; #pragma unroll
;     for (int dd = 0; dd < 4; ++dd) kb[dd] = K_lds + KB * SHM_K + r32 * ROWB + (((dd * 16 + hi * 8) * 2) ^ ((r32 & 7) << 4));
; template <int DQK, bool BIAS> ...
;     ...
;     const int tid = threadIdx.x, wid = __builtin_amdgcn_readfirstlane(tid >> 6), lane = tid & 63, r32 = lane & 31, hi = lane >> 5;
;     char* V_lds = lds; char* K_lds = lds + NRING * SHM_V;
;     float* ws = (float*)(lds + NRING * SHM_V + NRING * SHM_K) + wid * 64; float* al_l = ws + 32;
;     const int sr = tid >> 4, sc = (tid & 15) * 8, vst0 = v_st(sr, sc), vst1 = v_st(32 + sr, sc), kws = sr * ROWB + ((sc * 2) ^ ((sr & 7) << 4));
;     const int rr_ = tid >> 3, rc = (tid & 7) * 8, kws2 = rr_ * ROWB + 256 + ((rc * 2) ^ ((rr_ & 7) << 4));
;     const int vb0 = (int)(uintptr_t)V_lds + v_rd_base(lane);
;     const unsigned goff = (unsigned)(sr * (int)kpitch + sc) * 2u, goff2 = (unsigned)(rr_ * 64 + rc) * 2u;
.LBB0_783:
	v_lshlrev_b32_e32 v4, 3, v0
	v_lshlrev_b32_e32 v13, 4, v0
	v_lshlrev_b32_e32 v16, 1, v0
	v_and_b32_e32 v5, 0x78, v4
	v_bfe_u32 v10, v4, 5, 2
	v_and_b32_e32 v15, 0xc0, v13
	v_and_b32_e32 v16, 32, v16
	v_and_b32_e32 v4, 0x118, v4
	s_cmp_lg_u32 0, -1
	v_lshrrev_b32_e32 v2, 5, v170
	v_or3_b32 v4, v16, v15, v4
	s_cselect_b32 s3, 0, 0
	s_add_i32 s5, 0, 0x12000
	s_movk_i32 s4, 0x180
	v_and_b32_e32 v171, 31, v0
	v_add_u32_e32 v181, s3, v4
	v_lshlrev_b32_e32 v4, 4, v2
	v_lshlrev_b32_e32 v187, 2, v2
	v_mov_b32_e32 v2, s5
	s_add_i32 s33, 0, 0x18000
	v_mad_u32_u24 v188, v171, s4, v2
	v_mov_b32_e32 v2, s33
	v_mad_u32_u24 v182, v171, s4, 0
	v_mad_u32_u24 v189, v171, s4, v2
	s_lshl_b32 s4, s6, 2
	s_add_i32 s82, s4, 0
	s_add_i32 s82, s82, 0x1e000
	v_lshrrev_b32_e32 v3, 4, v0
	v_lshrrev_b32_e32 v6, 3, v0
	s_add_u32 s70, s94, 0x40c00000
	v_and_b32_e32 v7, 8, v6
	v_or_b32_e32 v12, 32, v3
	s_addc_u32 s71, s95, 0
	v_and_or_b32 v8, v3, 16, v7
	v_and_or_b32 v7, v12, 48, v7
	s_add_u32 s4, s94, 0x43c00000
	v_lshrrev_b32_e32 v9, 5, v0
	v_lshrrev_b32_e32 v8, 1, v8
	v_bfe_u32 v11, v0, 4, 2
	v_lshrrev_b32_e32 v7, 1, v7
	v_writelane_b32 v255, s4, 18
	s_addc_u32 s4, s95, 0
	v_or_b32_e32 v8, v8, v10
	v_and_or_b32 v9, v9, 4, v11
	v_lshlrev_b32_e32 v5, 1, v5
	v_or_b32_e32 v7, v7, v10
	v_writelane_b32 v255, s4, 15
	s_add_u32 s4, s94, 0x40900000
	v_lshlrev_b32_e32 v8, 9, v8
	v_lshlrev_b32_e32 v9, 6, v9
	v_and_b32_e32 v11, 48, v5
	v_lshlrev_b32_e32 v7, 9, v7
	v_xor_b32_e32 v14, v3, v0
	v_writelane_b32 v255, s4, 20
	s_addc_u32 s4, s95, 0
	v_or3_b32 v7, v7, v9, v11
	s_movk_i32 s2, 0x70
	v_lshrrev_b32_e32 v10, 1, v0
	v_and_b32_e32 v10, 0x70, v10
	v_mul_u32_u24_e32 v12, 0x180, v6
	v_lshlrev_b32_e32 v14, 4, v14
	v_or3_b32 v8, v8, v9, v11
	v_mul_u32_u24_e32 v9, 0x180, v3
	v_writelane_b32 v255, s4, 19
	v_readlane_b32 s4, v254, 38
	v_xad_u32 v173, v5, v10, v9
	v_and_or_b32 v10, v14, s2, v12
	v_sub_u32_e32 v2, s4, v187
	v_and_b32_e32 v9, 0x70, v13
	v_add_u32_e32 v180, 0x100, v10
	v_lshl_or_b32 v174, v3, 12, v5
	v_mov_b32_e32 v3, 0
	v_lshlrev_b32_e32 v20, 3, v0
	v_and_b32_e32 v21, 0x70, v20
	v_bitop3_b32 v183, v4, v20, s2 bitop3:0x78
	s_movk_i32 s2, 0x60
	v_add_u32_e32 v190, 0x1f00, v2
	s_add_i32 s4, 0, 0x20040
	v_mbcnt_lo_u32_b32 v2, -1, 0
	s_mov_b32 s69, 0
	v_cmp_eq_u32_e64 s[0:1], 0, v0
	v_lshl_or_b32 v176, v6, 7, v9
	v_mov_b32_e32 v175, v3
	v_mov_b32_e32 v177, v3
	v_bitop3_b32 v184, v4, v21, 32 bitop3:0x36
	v_bitop3_b32 v185, v4, v21, 64 bitop3:0x36
	v_bitop3_b32 v186, v4, v21, s2 bitop3:0x36
	v_cmp_gt_u32_e64 s[2:3], 32, v170
	v_writelane_b32 v254, s4, 62
	v_mov_b32_e32 v191, s4
	s_mov_b32 s96, 0x20000
	v_add_u32_e32 v192, 0, v173
	v_add_u32_e32 v193, 0, v10
	v_add_u32_e32 v194, 0, v8
	v_add_u32_e32 v195, 0, v7
	v_add_u32_e32 v196, s5, v173
	v_add_u32_e32 v197, s5, v180
	s_mov_b64 s[72:73], 0x20000
	s_mov_b32 s97, 0x41000000
	v_mov_b32_e32 v198, 0xff800000
	v_mbcnt_hi_u32_b32 v199, -1, v2
	s_branch .LBB0_786

; #define PG8_STAGE(bufoff, gbase, voff) do { _Pragma("unroll") for (int _i = 0; _i < 2; ++_i) \
;         __builtin_amdgcn_global_load_lds((const unsigned*)((const char*)(gbase) + (voff)[_i]), (LAS unsigned*)(lds + (bufoff) + ldsw + _i * 8192), 16, 0, 0); } while (0)
; #define PG8_LDA(dst, b, h) do { if constexpr (FP8) { _Pragma("unroll") for (int m = 0; m < 4; ++m) dst##8[m] = PG8_LD8(lds + PG8_SA(b, h) + aoff + m * 2048); } \
;         else { _Pragma("unroll") for (int m = 0; m < 4; ++m) _Pragma("unroll") for (int k = 0; k < 2; ++k) dst[m][k] = *(const LAS bf16x8*)(lds + PG8_SA(b, h) + aoff + m * 2048 + k * 1024); } } while (0)
; #define PG8_LDB(dst, b, h) do { if constexpr (FP8) { _Pragma("unroll") for (int n = 0; n < 2; ++n) dst##8[n] = PG8_LD8(lds + PG8_SB(b, h) + boff + n * 2048); } \
;         else { _Pragma("unroll") for (int n = 0; n < 2; ++n) _Pragma("unroll") for (int k = 0; k < 2; ++k) dst[n][k] = *(const LAS bf16x8*)(lds + PG8_SB(b, h) + boff + n * 2048 + k * 1024); } } while (0)
; #define PG8_WAIT_V(n) asm volatile("s_waitcnt vmcnt(" #n ")" ::: "memory")
; #define PG8_WAIT_L(n) asm volatile("s_waitcnt lgkmcnt(" #n ")" ::: "memory")
; #define PG8_BAR __builtin_amdgcn_s_barrier()
; #define PG8_SCHED __builtin_amdgcn_sched_barrier(0)
; template <class Epi, class Sched, bool GATHER, bool FP8 = false>
; __device__ __forceinline__ void gemm_phase(LAS unsigned char* lds, const Gemm g, const Sched& S, const Epi& E) {
;     ...
;         for (int t = 0; t < nt; t += 2) {
;             const bool last = (t == nt - 2);
;             const char* a1 = cA + (size_t)(t + 1) * kstep;
;             const char* a2 = last ? nA : cA + (size_t)(t + 2) * kstep; const char* b2 = last ? nB : cB + (size_t)(t + 2) * kstep;
;             const char* a3 = a2 + kstep; const char* b3 = b2 + kstep;
;             PG8_LDB(B0, 0, 0); PG8_LDB(B1, 0, 1); PG8_SCHED; PG8_LDA(At, 0, 0); PG8_STAGE_A(PG8_SA(1, 1), a1, 1, false);
;             PG8_WAIT_V(8); PG8_WAIT_L(0); PG8_BAR; PG8_MMA(0, 0, At, B0); PG8_MMA(0, 1, At, B1); PG8_BAR; PG8_SCHED;
;             PG8_LDA(At, 0, 1); PG8_STAGE(PG8_SB(0, 0), b2, voffB); PG8_STAGE(PG8_SB(0, 1), b2 + hstep, voffB); PG8_STAGE_A(PG8_SA(0, 0), a2, 0, last);
;             PG8_WAIT_V(8); PG8_WAIT_L(0); PG8_BAR; PG8_MMA(1, 0, At, B0); PG8_MMA(1, 1, At, B1); PG8_BAR; PG8_SCHED;
.LBB0_1428:
	ds_read_b128 v[18:21], v201
	ds_read_b128 v[22:25], v201 offset:1024
	ds_read_b128 v[26:29], v201 offset:2048
	ds_read_b128 v[30:33], v201 offset:3072
	ds_read_b128 v[2:5], v202
	ds_read_b128 v[6:9], v202 offset:1024
	ds_read_b128 v[10:13], v202 offset:2048
	ds_read_b128 v[14:17], v202 offset:3072
	s_add_u32 s26, s30, 0x100
	s_addc_u32 s27, s31, 0
	s_add_u32 s34, s23, s30
	s_addc_u32 s35, s25, s31
	s_cmpk_eq_i32 s30, 0x700
	s_cselect_b64 vcc, -1, 0
	s_and_b64 s[28:29], vcc, exec
	s_cselect_b32 s64, 0, s26
	s_cselect_b32 s63, 0, s27
	s_cselect_b32 s28, s2, s34
	s_cselect_b32 s29, s3, s35
	s_add_u32 s34, s6, s64
	s_addc_u32 s35, s7, s63
	v_lshl_add_u64 v[234:235], v[188:189], 0, s[30:31]
	s_add_i32 m0, s39, 0xc000
	ds_read_b128 v[190:193], v203
	ds_read_b128 v[194:197], v203 offset:1024
	ds_read_b128 v[210:213], v203 offset:2048
	ds_read_b128 v[214:217], v203 offset:3072
	ds_read_b128 v[218:221], v203 offset:4096
	ds_read_b128 v[222:225], v203 offset:5120
	ds_read_b128 v[226:229], v203 offset:6144
	ds_read_b128 v[230:233], v203 offset:7168
	global_load_lds_dwordx4 v[234:235], off
	v_lshl_add_u64 v[234:235], v[186:187], 0, s[30:31]
	s_add_i32 m0, s39, 0xe000
	s_nop 0
	global_load_lds_dwordx4 v[234:235], off
	s_waitcnt vmcnt(8)
	s_waitcnt lgkmcnt(0)
	s_barrier
	s_setprio 1
	s_waitcnt lgkmcnt(0)
	v_mfma_f32_16x16x128_f8f6f4 v[158:161], v[18:25], v[190:197], v[158:161]
	v_mfma_f32_16x16x128_f8f6f4 v[150:153], v[26:33], v[190:197], v[150:153]
	v_mfma_f32_16x16x128_f8f6f4 v[142:145], v[18:25], v[210:217], v[142:145]
	v_mfma_f32_16x16x128_f8f6f4 v[134:137], v[26:33], v[210:217], v[134:137]
	v_mfma_f32_16x16x128_f8f6f4 v[126:129], v[18:25], v[218:225], v[126:129]
	v_mfma_f32_16x16x128_f8f6f4 v[118:121], v[26:33], v[218:225], v[118:121]
	v_mfma_f32_16x16x128_f8f6f4 v[110:113], v[18:25], v[226:233], v[110:113]
	v_mfma_f32_16x16x128_f8f6f4 v[102:105], v[26:33], v[226:233], v[102:105]
	s_setprio 0
	s_setprio 1
	v_mfma_f32_16x16x128_f8f6f4 v[154:157], v[2:9], v[190:197], v[154:157]
	v_mfma_f32_16x16x128_f8f6f4 v[146:149], v[10:17], v[190:197], v[146:149]
	v_mfma_f32_16x16x128_f8f6f4 v[138:141], v[2:9], v[210:217], v[138:141]
	v_mfma_f32_16x16x128_f8f6f4 v[130:133], v[10:17], v[210:217], v[130:133]
	v_mfma_f32_16x16x128_f8f6f4 v[122:125], v[2:9], v[218:225], v[122:125]
	v_mfma_f32_16x16x128_f8f6f4 v[114:117], v[10:17], v[218:225], v[114:117]
	v_mfma_f32_16x16x128_f8f6f4 v[106:109], v[2:9], v[226:233], v[106:109]
	v_mfma_f32_16x16x128_f8f6f4 v[98:101], v[10:17], v[226:233], v[98:101]
	s_setprio 0
	s_barrier
	s_add_i32 s30, s52, s38
	v_lshl_add_u64 v[190:191], s[28:29], 0, v[168:169]
	s_mov_b32 m0, s30
	ds_read_b128 v[210:213], v203 offset:16384
	ds_read_b128 v[214:217], v203 offset:17408
	ds_read_b128 v[218:221], v203 offset:18432
	ds_read_b128 v[222:225], v203 offset:19456
	ds_read_b128 v[226:229], v203 offset:20480
	ds_read_b128 v[230:233], v203 offset:21504
	ds_read_b128 v[234:237], v203 offset:22528
	ds_read_b128 v[238:241], v203 offset:23552
	global_load_lds_dwordx4 v[190:191], off
	s_add_i32 m0, s30, 0x2000
	s_add_u32 s30, s28, 0x40000
	v_lshl_add_u64 v[192:193], s[28:29], 0, v[172:173]
	s_addc_u32 s31, s29, 0
	s_add_i32 s63, s53, s38
	global_load_lds_dwordx4 v[192:193], off
	v_lshl_add_u64 v[194:195], s[30:31], 0, v[168:169]
	s_mov_b32 m0, s63
	v_cndmask_b32_e32 v164, v209, v206, vcc
	global_load_lds_dwordx4 v[194:195], off
	v_lshl_add_u64 v[194:195], s[30:31], 0, v[172:173]
	s_add_i32 m0, s63, 0x2000
	s_nop 0
	global_load_lds_dwordx4 v[194:195], off
	v_lshl_add_u64 v[194:195], s[34:35], 0, v[164:165]
	v_cndmask_b32_e32 v164, v180, v205, vcc
	v_lshl_add_u64 v[194:195], v[194:195], 0, v[166:167]
	s_mov_b32 m0, s39
	v_lshl_add_u64 v[196:197], s[34:35], 0, v[164:165]
	global_load_lds_dwordx4 v[194:195], off
	v_lshl_add_u64 v[196:197], v[196:197], 0, v[166:167]
	s_mov_b32 m0, s40
	s_nop 0
	global_load_lds_dwordx4 v[196:197], off
	s_waitcnt vmcnt(8)
	s_waitcnt lgkmcnt(0)
	s_barrier
	s_setprio 1
	s_waitcnt lgkmcnt(0)
	v_mfma_f32_16x16x128_f8f6f4 v[94:97], v[18:25], v[210:217], v[94:97]
	v_mfma_f32_16x16x128_f8f6f4 v[86:89], v[26:33], v[210:217], v[86:89]
	v_mfma_f32_16x16x128_f8f6f4 v[78:81], v[18:25], v[218:225], v[78:81]
	v_mfma_f32_16x16x128_f8f6f4 v[70:73], v[26:33], v[218:225], v[70:73]
	v_mfma_f32_16x16x128_f8f6f4 v[62:65], v[18:25], v[226:233], v[62:65]
	v_mfma_f32_16x16x128_f8f6f4 v[54:57], v[26:33], v[226:233], v[54:57]
	v_mfma_f32_16x16x128_f8f6f4 v[46:49], v[18:25], v[234:241], v[46:49]
	v_mfma_f32_16x16x128_f8f6f4 v[38:41], v[26:33], v[234:241], v[38:41]
	s_setprio 0
	s_setprio 1
	v_mfma_f32_16x16x128_f8f6f4 v[90:93], v[2:9], v[210:217], v[90:93]
	v_mfma_f32_16x16x128_f8f6f4 v[82:85], v[10:17], v[210:217], v[82:85]
	v_mfma_f32_16x16x128_f8f6f4 v[74:77], v[2:9], v[218:225], v[74:77]
	v_mfma_f32_16x16x128_f8f6f4 v[66:69], v[10:17], v[218:225], v[66:69]
	v_mfma_f32_16x16x128_f8f6f4 v[58:61], v[2:9], v[226:233], v[58:61]
	v_mfma_f32_16x16x128_f8f6f4 v[50:53], v[10:17], v[226:233], v[50:53]
	v_mfma_f32_16x16x128_f8f6f4 v[42:45], v[2:9], v[234:241], v[42:45]
	v_mfma_f32_16x16x128_f8f6f4 v[34:37], v[10:17], v[234:241], v[34:37]
	s_setprio 0
	s_barrier
; #define PG8_STAGE(bufoff, gbase, voff) do { _Pragma("unroll") for (int _i = 0; _i < 2; ++_i) \
;         __builtin_amdgcn_global_load_lds((const unsigned*)((const char*)(gbase) + (voff)[_i]), (LAS unsigned*)(lds + (bufoff) + ldsw + _i * 8192), 16, 0, 0); } while (0)
; #define PG8_LDA(dst, b, h) do { if constexpr (FP8) { _Pragma("unroll") for (int m = 0; m < 4; ++m) dst##8[m] = PG8_LD8(lds + PG8_SA(b, h) + aoff + m * 2048); } \
;         else { _Pragma("unroll") for (int m = 0; m < 4; ++m) _Pragma("unroll") for (int k = 0; k < 2; ++k) dst[m][k] = *(const LAS bf16x8*)(lds + PG8_SA(b, h) + aoff + m * 2048 + k * 1024); } } while (0)
; #define PG8_LDB(dst, b, h) do { if constexpr (FP8) { _Pragma("unroll") for (int n = 0; n < 2; ++n) dst##8[n] = PG8_LD8(lds + PG8_SB(b, h) + boff + n * 2048); } \
;         else { _Pragma("unroll") for (int n = 0; n < 2; ++n) _Pragma("unroll") for (int k = 0; k < 2; ++k) dst[n][k] = *(const LAS bf16x8*)(lds + PG8_SB(b, h) + boff + n * 2048 + k * 1024); } } while (0)
; #define PG8_WAIT_V(n) asm volatile("s_waitcnt vmcnt(" #n ")" ::: "memory")
; #define PG8_WAIT_L(n) asm volatile("s_waitcnt lgkmcnt(" #n ")" ::: "memory")
; #define PG8_BAR __builtin_amdgcn_s_barrier()
; #define PG8_SCHED __builtin_amdgcn_sched_barrier(0)
; template <class Epi, class Sched, bool GATHER, bool FP8 = false>
; __device__ __forceinline__ void gemm_phase(LAS unsigned char* lds, const Gemm g, const Sched& S, const Epi& E) {
;     ...
;             PG8_LDB(B0, 1, 0); PG8_LDB(B1, 1, 1); PG8_SCHED; PG8_LDA(At, 1, 0); PG8_STAGE_A(PG8_SA(0, 1), a2, 1, last);
;             PG8_WAIT_V(8); PG8_WAIT_L(0); PG8_BAR; PG8_MMA(0, 0, At, B0); PG8_MMA(0, 1, At, B1); PG8_BAR; PG8_SCHED;
;             PG8_LDA(At, 1, 1); PG8_STAGE(PG8_SB(1, 0), b3, voffB); PG8_STAGE(PG8_SB(1, 1), b3 + hstep, voffB); PG8_STAGE_A(PG8_SA(1, 0), a3, 0, last);
;             PG8_WAIT_V(8); PG8_WAIT_L(0); PG8_BAR; PG8_MMA(1, 0, At, B0); PG8_MMA(1, 1, At, B1); PG8_BAR; PG8_SCHED;
;         }
;         if constexpr (FP8) asm volatile("s_nop 15\n\ts_nop 15" ::: "memory");
;         if (wr == 0) PG8_BAR;
	s_add_i32 s30, 0, 0x18000
	s_add_i32 s31, 0, 0x1c000
	v_add_u32_e32 v14, s30, v200
	v_add_u32_e32 v30, s31, v200
	ds_read_b128 v[2:5], v14
	ds_read_b128 v[6:9], v14 offset:1024
	ds_read_b128 v[10:13], v14 offset:2048
	ds_read_b128 v[14:17], v14 offset:3072
	ds_read_b128 v[18:21], v30
	ds_read_b128 v[22:25], v30 offset:1024
	ds_read_b128 v[26:29], v30 offset:2048
	ds_read_b128 v[30:33], v30 offset:3072
	v_cndmask_b32_e32 v164, v184, v208, vcc
	v_lshl_add_u64 v[242:243], s[34:35], 0, v[164:165]
	s_mov_b32 m0, s41
	v_lshl_add_u64 v[242:243], v[242:243], 0, v[166:167]
	v_cndmask_b32_e32 v164, v182, v207, vcc
	ds_read_b128 v[210:213], v203 offset:32768
	ds_read_b128 v[214:217], v203 offset:33792
	ds_read_b128 v[218:221], v203 offset:34816
	ds_read_b128 v[222:225], v203 offset:35840
	ds_read_b128 v[226:229], v203 offset:36864
	ds_read_b128 v[230:233], v203 offset:37888
	ds_read_b128 v[234:237], v203 offset:38912
	ds_read_b128 v[238:241], v203 offset:39936
	global_load_lds_dwordx4 v[242:243], off
	v_lshl_add_u64 v[242:243], s[34:35], 0, v[164:165]
	v_lshl_add_u64 v[242:243], v[242:243], 0, v[166:167]
	s_mov_b32 m0, s42
	s_nop 0
	global_load_lds_dwordx4 v[242:243], off
	s_waitcnt vmcnt(8)
	s_waitcnt lgkmcnt(0)
	s_barrier
	s_setprio 1
	s_waitcnt lgkmcnt(0)
	v_mfma_f32_16x16x128_f8f6f4 v[158:161], v[2:9], v[210:217], v[158:161]
	v_mfma_f32_16x16x128_f8f6f4 v[150:153], v[10:17], v[210:217], v[150:153]
	v_mfma_f32_16x16x128_f8f6f4 v[142:145], v[2:9], v[218:225], v[142:145]
	v_mfma_f32_16x16x128_f8f6f4 v[134:137], v[10:17], v[218:225], v[134:137]
	v_mfma_f32_16x16x128_f8f6f4 v[126:129], v[2:9], v[226:233], v[126:129]
	v_mfma_f32_16x16x128_f8f6f4 v[118:121], v[10:17], v[226:233], v[118:121]
	v_mfma_f32_16x16x128_f8f6f4 v[110:113], v[2:9], v[234:241], v[110:113]
	v_mfma_f32_16x16x128_f8f6f4 v[102:105], v[10:17], v[234:241], v[102:105]
	s_setprio 0
	s_setprio 1
	v_mfma_f32_16x16x128_f8f6f4 v[154:157], v[18:25], v[210:217], v[154:157]
	v_mfma_f32_16x16x128_f8f6f4 v[146:149], v[26:33], v[210:217], v[146:149]
	v_mfma_f32_16x16x128_f8f6f4 v[138:141], v[18:25], v[218:225], v[138:141]
	v_mfma_f32_16x16x128_f8f6f4 v[130:133], v[26:33], v[218:225], v[130:133]
	v_mfma_f32_16x16x128_f8f6f4 v[122:125], v[18:25], v[226:233], v[122:125]
	v_mfma_f32_16x16x128_f8f6f4 v[114:117], v[26:33], v[226:233], v[114:117]
	v_mfma_f32_16x16x128_f8f6f4 v[106:109], v[18:25], v[234:241], v[106:109]
	v_mfma_f32_16x16x128_f8f6f4 v[98:101], v[26:33], v[234:241], v[98:101]
	s_setprio 0
	s_barrier
	s_add_i32 s30, s30, s38
	v_lshl_add_u64 v[190:191], v[190:191], 0, s[12:13]
	s_mov_b32 m0, s30
	ds_read_b128 v[210:213], v203 offset:49152
	ds_read_b128 v[214:217], v203 offset:50176
	ds_read_b128 v[218:221], v203 offset:51200
	ds_read_b128 v[222:225], v203 offset:52224
	ds_read_b128 v[226:229], v203 offset:53248
	ds_read_b128 v[230:233], v203 offset:54272
	ds_read_b128 v[234:237], v203 offset:55296
	ds_read_b128 v[238:241], v203 offset:56320
	global_load_lds_dwordx4 v[190:191], off
	s_add_i32 m0, s30, 0x2000
	s_add_u32 s28, s28, 0x40080
	v_lshl_add_u64 v[190:191], v[192:193], 0, s[12:13]
	s_addc_u32 s29, s29, 0
	s_add_i32 s30, s31, s38
	global_load_lds_dwordx4 v[190:191], off
	v_lshl_add_u64 v[190:191], s[28:29], 0, v[168:169]
	s_mov_b32 m0, s30
	s_nop 0
	global_load_lds_dwordx4 v[190:191], off
	v_lshl_add_u64 v[190:191], s[28:29], 0, v[172:173]
	s_add_i32 m0, s30, 0x2000
	s_nop 0
	global_load_lds_dwordx4 v[190:191], off
	v_lshl_add_u64 v[190:191], v[194:195], 0, s[12:13]
	s_mov_b32 m0, s46
	s_nop 0
	global_load_lds_dwordx4 v[190:191], off
	v_lshl_add_u64 v[190:191], v[196:197], 0, s[12:13]
	s_mov_b32 m0, s47
	s_nop 0
	global_load_lds_dwordx4 v[190:191], off
	s_waitcnt vmcnt(8)
	s_waitcnt lgkmcnt(0)
	s_barrier
	s_setprio 1
	s_waitcnt lgkmcnt(0)
	v_mfma_f32_16x16x128_f8f6f4 v[94:97], v[2:9], v[210:217], v[94:97]
	v_mfma_f32_16x16x128_f8f6f4 v[86:89], v[10:17], v[210:217], v[86:89]
	v_mfma_f32_16x16x128_f8f6f4 v[78:81], v[2:9], v[218:225], v[78:81]
	v_mfma_f32_16x16x128_f8f6f4 v[70:73], v[10:17], v[218:225], v[70:73]
	v_mfma_f32_16x16x128_f8f6f4 v[62:65], v[2:9], v[226:233], v[62:65]
	v_mfma_f32_16x16x128_f8f6f4 v[54:57], v[10:17], v[226:233], v[54:57]
	v_mfma_f32_16x16x128_f8f6f4 v[46:49], v[2:9], v[234:241], v[46:49]
	v_mfma_f32_16x16x128_f8f6f4 v[38:41], v[10:17], v[234:241], v[38:41]
	s_setprio 0
	s_setprio 1
	v_mfma_f32_16x16x128_f8f6f4 v[90:93], v[18:25], v[210:217], v[90:93]
	v_mfma_f32_16x16x128_f8f6f4 v[82:85], v[26:33], v[210:217], v[82:85]
	v_mfma_f32_16x16x128_f8f6f4 v[74:77], v[18:25], v[218:225], v[74:77]
	v_mfma_f32_16x16x128_f8f6f4 v[66:69], v[26:33], v[218:225], v[66:69]
	v_mfma_f32_16x16x128_f8f6f4 v[58:61], v[18:25], v[226:233], v[58:61]
	v_mfma_f32_16x16x128_f8f6f4 v[50:53], v[26:33], v[226:233], v[50:53]
	v_mfma_f32_16x16x128_f8f6f4 v[42:45], v[18:25], v[234:241], v[42:45]
	v_mfma_f32_16x16x128_f8f6f4 v[34:37], v[26:33], v[234:241], v[34:37]
	s_setprio 0
	s_barrier
	s_add_i32 s62, s62, 2
	s_cmp_gt_u32 s62, 13
	s_mov_b64 s[30:31], s[26:27]
	s_cbranch_scc0 .LBB0_1428
	s_nop 15
	s_nop 15
	s_and_b64 vcc, exec, s[14:15]
	s_cbranch_vccz .LBB0_1431
	s_barrier

; #define PG8_STAGE(bufoff, gbase, voff) do { _Pragma("unroll") for (int _i = 0; _i < 2; ++_i) \
;         __builtin_amdgcn_global_load_lds((const unsigned*)((const char*)(gbase) + (voff)[_i]), (LAS unsigned*)(lds + (bufoff) + ldsw + _i * 8192), 16, 0, 0); } while (0)
; #define PG8_LDA(dst, b, h) do { if constexpr (FP8) { _Pragma("unroll") for (int m = 0; m < 4; ++m) dst##8[m] = PG8_LD8(lds + PG8_SA(b, h) + aoff + m * 2048); } \
;         else { _Pragma("unroll") for (int m = 0; m < 4; ++m) _Pragma("unroll") for (int k = 0; k < 2; ++k) dst[m][k] = *(const LAS bf16x8*)(lds + PG8_SA(b, h) + aoff + m * 2048 + k * 1024); } } while (0)
; #define PG8_LDB(dst, b, h) do { if constexpr (FP8) { _Pragma("unroll") for (int n = 0; n < 2; ++n) dst##8[n] = PG8_LD8(lds + PG8_SB(b, h) + boff + n * 2048); } \
;         else { _Pragma("unroll") for (int n = 0; n < 2; ++n) _Pragma("unroll") for (int k = 0; k < 2; ++k) dst[n][k] = *(const LAS bf16x8*)(lds + PG8_SB(b, h) + boff + n * 2048 + k * 1024); } } while (0)
; #define PG8_WAIT_V(n) asm volatile("s_waitcnt vmcnt(" #n ")" ::: "memory")
; #define PG8_WAIT_L(n) asm volatile("s_waitcnt lgkmcnt(" #n ")" ::: "memory")
; #define PG8_BAR __builtin_amdgcn_s_barrier()
; #define PG8_SCHED __builtin_amdgcn_sched_barrier(0)
; template <class Epi, class Sched, bool GATHER, bool FP8 = false>
; __device__ __forceinline__ void gemm_phase(LAS unsigned char* lds, const Gemm g, const Sched& S, const Epi& E) {
;     ...
;         for (int t = 0; t < nt; t += 2) {
;             const bool last = (t == nt - 2);
;             const char* a1 = cA + (size_t)(t + 1) * kstep;
;             const char* a2 = last ? nA : cA + (size_t)(t + 2) * kstep; const char* b2 = last ? nB : cB + (size_t)(t + 2) * kstep;
;             const char* a3 = a2 + kstep; const char* b3 = b2 + kstep;
;             PG8_LDB(B0, 0, 0); PG8_LDB(B1, 0, 1); PG8_SCHED; PG8_LDA(At, 0, 0); PG8_STAGE_A(PG8_SA(1, 1), a1, 1, false);
;             PG8_WAIT_V(8); PG8_WAIT_L(0); PG8_BAR; PG8_MMA(0, 0, At, B0); PG8_MMA(0, 1, At, B1); PG8_BAR; PG8_SCHED;
;             PG8_LDA(At, 0, 1); PG8_STAGE(PG8_SB(0, 0), b2, voffB); PG8_STAGE(PG8_SB(0, 1), b2 + hstep, voffB); PG8_STAGE_A(PG8_SA(0, 0), a2, 0, last);
;             PG8_WAIT_V(8); PG8_WAIT_L(0); PG8_BAR; PG8_MMA(1, 0, At, B0); PG8_MMA(1, 1, At, B1); PG8_BAR; PG8_SCHED;
.LBB0_1521:
	ds_read_b128 v[18:21], v190
	ds_read_b128 v[22:25], v190 offset:1024
	ds_read_b128 v[26:29], v190 offset:2048
	ds_read_b128 v[30:33], v190 offset:3072
	ds_read_b128 v[2:5], v191
	ds_read_b128 v[6:9], v191 offset:1024
	ds_read_b128 v[10:13], v191 offset:2048
	ds_read_b128 v[14:17], v191 offset:3072
	s_add_u32 s40, s6, 0xfffc0080
	s_addc_u32 s41, s7, -1
	s_cmp_eq_u32 s61, 12
	s_cselect_b32 s43, s23, s41
	s_cselect_b32 s42, s25, s40
	s_cselect_b32 s41, s29, s39
	s_cselect_b32 s40, s28, s27
	v_lshl_add_u64 v[218:219], s[6:7], 0, v[176:177]
	s_add_i32 m0, s35, 0xc000
	ds_read_b128 v[180:183], v192
	ds_read_b128 v[184:187], v192 offset:1024
	ds_read_b128 v[194:197], v192 offset:2048
	ds_read_b128 v[198:201], v192 offset:3072
	ds_read_b128 v[202:205], v192 offset:4096
	ds_read_b128 v[206:209], v192 offset:5120
	ds_read_b128 v[210:213], v192 offset:6144
	ds_read_b128 v[214:217], v192 offset:7168
	global_load_lds_dwordx4 v[218:219], off
	v_lshl_add_u64 v[218:219], s[6:7], 0, v[178:179]
	s_add_i32 m0, s35, 0xe000
	s_nop 0
	global_load_lds_dwordx4 v[218:219], off
	s_waitcnt vmcnt(8)
	s_waitcnt lgkmcnt(0)
	s_barrier
	s_setprio 1
	s_waitcnt lgkmcnt(0)
	v_mfma_f32_16x16x128_f8f6f4 v[158:161], v[18:25], v[180:187], v[158:161]
	v_mfma_f32_16x16x128_f8f6f4 v[154:157], v[26:33], v[180:187], v[154:157]
	v_mfma_f32_16x16x128_f8f6f4 v[142:145], v[18:25], v[194:201], v[142:145]
	v_mfma_f32_16x16x128_f8f6f4 v[138:141], v[26:33], v[194:201], v[138:141]
	v_mfma_f32_16x16x128_f8f6f4 v[126:129], v[18:25], v[202:209], v[126:129]
	v_mfma_f32_16x16x128_f8f6f4 v[122:125], v[26:33], v[202:209], v[122:125]
	v_mfma_f32_16x16x128_f8f6f4 v[110:113], v[18:25], v[210:217], v[110:113]
	v_mfma_f32_16x16x128_f8f6f4 v[106:109], v[26:33], v[210:217], v[106:109]
	s_setprio 0
	s_setprio 1
	v_mfma_f32_16x16x128_f8f6f4 v[150:153], v[2:9], v[180:187], v[150:153]
	v_mfma_f32_16x16x128_f8f6f4 v[146:149], v[10:17], v[180:187], v[146:149]
	v_mfma_f32_16x16x128_f8f6f4 v[134:137], v[2:9], v[194:201], v[134:137]
	v_mfma_f32_16x16x128_f8f6f4 v[130:133], v[10:17], v[194:201], v[130:133]
	v_mfma_f32_16x16x128_f8f6f4 v[118:121], v[2:9], v[202:209], v[118:121]
	v_mfma_f32_16x16x128_f8f6f4 v[114:117], v[10:17], v[202:209], v[114:117]
	v_mfma_f32_16x16x128_f8f6f4 v[102:105], v[2:9], v[210:217], v[102:105]
	v_mfma_f32_16x16x128_f8f6f4 v[98:101], v[10:17], v[210:217], v[98:101]
	s_setprio 0
	s_barrier
	s_add_i32 s62, s56, s47
	v_lshl_add_u64 v[180:181], s[40:41], 0, v[166:167]
	s_mov_b32 m0, s62
	ds_read_b128 v[194:197], v192 offset:16384
	ds_read_b128 v[198:201], v192 offset:17408
	ds_read_b128 v[202:205], v192 offset:18432
	ds_read_b128 v[206:209], v192 offset:19456
	ds_read_b128 v[210:213], v192 offset:20480
	ds_read_b128 v[214:217], v192 offset:21504
	ds_read_b128 v[218:221], v192 offset:22528
	ds_read_b128 v[222:225], v192 offset:23552
	global_load_lds_dwordx4 v[180:181], off
	s_add_i32 m0, s62, 0x2000
	s_add_u32 s62, s40, 0x40000
	v_lshl_add_u64 v[182:183], s[40:41], 0, v[172:173]
	s_addc_u32 s63, s41, 0
	s_add_i32 s64, s57, s47
	global_load_lds_dwordx4 v[182:183], off
	v_lshl_add_u64 v[184:185], s[62:63], 0, v[166:167]
	s_mov_b32 m0, s64
	v_lshl_add_u64 v[186:187], s[42:43], 0, v[168:169]
	global_load_lds_dwordx4 v[184:185], off
	v_lshl_add_u64 v[184:185], s[62:63], 0, v[172:173]
	s_add_i32 m0, s64, 0x2000
	s_nop 0
	global_load_lds_dwordx4 v[184:185], off
	v_lshl_add_u64 v[184:185], s[42:43], 0, v[164:165]
	s_mov_b32 m0, s35
	s_nop 0
	global_load_lds_dwordx4 v[184:185], off
	s_mov_b32 m0, s37
	s_nop 0
	global_load_lds_dwordx4 v[186:187], off
	s_waitcnt vmcnt(8)
	s_waitcnt lgkmcnt(0)
	s_barrier
	s_setprio 1
	s_waitcnt lgkmcnt(0)
	v_mfma_f32_16x16x128_f8f6f4 v[94:97], v[18:25], v[194:201], v[94:97]
	v_mfma_f32_16x16x128_f8f6f4 v[90:93], v[26:33], v[194:201], v[90:93]
	v_mfma_f32_16x16x128_f8f6f4 v[78:81], v[18:25], v[202:209], v[78:81]
	v_mfma_f32_16x16x128_f8f6f4 v[74:77], v[26:33], v[202:209], v[74:77]
	v_mfma_f32_16x16x128_f8f6f4 v[62:65], v[18:25], v[210:217], v[62:65]
	v_mfma_f32_16x16x128_f8f6f4 v[58:61], v[26:33], v[210:217], v[58:61]
	v_mfma_f32_16x16x128_f8f6f4 v[46:49], v[18:25], v[218:225], v[46:49]
	v_mfma_f32_16x16x128_f8f6f4 v[42:45], v[26:33], v[218:225], v[42:45]
	s_setprio 0
	s_setprio 1
	v_mfma_f32_16x16x128_f8f6f4 v[86:89], v[2:9], v[194:201], v[86:89]
	v_mfma_f32_16x16x128_f8f6f4 v[82:85], v[10:17], v[194:201], v[82:85]
	v_mfma_f32_16x16x128_f8f6f4 v[70:73], v[2:9], v[202:209], v[70:73]
	v_mfma_f32_16x16x128_f8f6f4 v[66:69], v[10:17], v[202:209], v[66:69]
	v_mfma_f32_16x16x128_f8f6f4 v[54:57], v[2:9], v[210:217], v[54:57]
	v_mfma_f32_16x16x128_f8f6f4 v[50:53], v[10:17], v[210:217], v[50:53]
	v_mfma_f32_16x16x128_f8f6f4 v[38:41], v[2:9], v[218:225], v[38:41]
	v_mfma_f32_16x16x128_f8f6f4 v[34:37], v[10:17], v[218:225], v[34:37]
	s_setprio 0
	s_barrier
; #define PG8_STAGE(bufoff, gbase, voff) do { _Pragma("unroll") for (int _i = 0; _i < 2; ++_i) \
;         __builtin_amdgcn_global_load_lds((const unsigned*)((const char*)(gbase) + (voff)[_i]), (LAS unsigned*)(lds + (bufoff) + ldsw + _i * 8192), 16, 0, 0); } while (0)
; #define PG8_LDA(dst, b, h) do { if constexpr (FP8) { _Pragma("unroll") for (int m = 0; m < 4; ++m) dst##8[m] = PG8_LD8(lds + PG8_SA(b, h) + aoff + m * 2048); } \
;         else { _Pragma("unroll") for (int m = 0; m < 4; ++m) _Pragma("unroll") for (int k = 0; k < 2; ++k) dst[m][k] = *(const LAS bf16x8*)(lds + PG8_SA(b, h) + aoff + m * 2048 + k * 1024); } } while (0)
; #define PG8_LDB(dst, b, h) do { if constexpr (FP8) { _Pragma("unroll") for (int n = 0; n < 2; ++n) dst##8[n] = PG8_LD8(lds + PG8_SB(b, h) + boff + n * 2048); } \
;         else { _Pragma("unroll") for (int n = 0; n < 2; ++n) _Pragma("unroll") for (int k = 0; k < 2; ++k) dst[n][k] = *(const LAS bf16x8*)(lds + PG8_SB(b, h) + boff + n * 2048 + k * 1024); } } while (0)
; #define PG8_WAIT_V(n) asm volatile("s_waitcnt vmcnt(" #n ")" ::: "memory")
; #define PG8_WAIT_L(n) asm volatile("s_waitcnt lgkmcnt(" #n ")" ::: "memory")
; #define PG8_BAR __builtin_amdgcn_s_barrier()
; #define PG8_SCHED __builtin_amdgcn_sched_barrier(0)
; template <class Epi, class Sched, bool GATHER, bool FP8 = false>
; __device__ __forceinline__ void gemm_phase(LAS unsigned char* lds, const Gemm g, const Sched& S, const Epi& E) {
;     ...
;             PG8_LDB(B0, 1, 0); PG8_LDB(B1, 1, 1); PG8_SCHED; PG8_LDA(At, 1, 0); PG8_STAGE_A(PG8_SA(0, 1), a2, 1, last);
;             PG8_WAIT_V(8); PG8_WAIT_L(0); PG8_BAR; PG8_MMA(0, 0, At, B0); PG8_MMA(0, 1, At, B1); PG8_BAR; PG8_SCHED;
;             PG8_LDA(At, 1, 1); PG8_STAGE(PG8_SB(1, 0), b3, voffB); PG8_STAGE(PG8_SB(1, 1), b3 + hstep, voffB); PG8_STAGE_A(PG8_SA(1, 0), a3, 0, last);
;             PG8_WAIT_V(8); PG8_WAIT_L(0); PG8_BAR; PG8_MMA(1, 0, At, B0); PG8_MMA(1, 1, At, B1); PG8_BAR; PG8_SCHED;
;         }
;         if constexpr (FP8) asm volatile("s_nop 15\n\ts_nop 15" ::: "memory");
;         if (wr == 0) PG8_BAR;
	s_add_i32 s62, 0, 0x18000
	s_add_i32 s63, 0, 0x1c000
	v_add_u32_e32 v14, s62, v189
	v_add_u32_e32 v30, s63, v189
	ds_read_b128 v[2:5], v14
	ds_read_b128 v[6:9], v14 offset:1024
	ds_read_b128 v[10:13], v14 offset:2048
	ds_read_b128 v[14:17], v14 offset:3072
	ds_read_b128 v[18:21], v30
	ds_read_b128 v[22:25], v30 offset:1024
	ds_read_b128 v[26:29], v30 offset:2048
	ds_read_b128 v[30:33], v30 offset:3072
	s_add_u32 s42, s42, 0x40000
	s_addc_u32 s43, s43, 0
	s_mov_b32 m0, s48
	v_lshl_add_u64 v[226:227], s[42:43], 0, v[164:165]
	ds_read_b128 v[194:197], v192 offset:32768
	ds_read_b128 v[198:201], v192 offset:33792
	ds_read_b128 v[202:205], v192 offset:34816
	ds_read_b128 v[206:209], v192 offset:35840
	ds_read_b128 v[210:213], v192 offset:36864
	ds_read_b128 v[214:217], v192 offset:37888
	ds_read_b128 v[218:221], v192 offset:38912
	ds_read_b128 v[222:225], v192 offset:39936
	global_load_lds_dwordx4 v[226:227], off
	v_lshl_add_u64 v[226:227], s[42:43], 0, v[168:169]
	s_mov_b32 m0, s49
	s_nop 0
	global_load_lds_dwordx4 v[226:227], off
	s_waitcnt vmcnt(8)
	s_waitcnt lgkmcnt(0)
	s_barrier
	s_setprio 1
	s_waitcnt lgkmcnt(0)
	v_mfma_f32_16x16x128_f8f6f4 v[158:161], v[2:9], v[194:201], v[158:161]
	v_mfma_f32_16x16x128_f8f6f4 v[154:157], v[10:17], v[194:201], v[154:157]
	v_mfma_f32_16x16x128_f8f6f4 v[142:145], v[2:9], v[202:209], v[142:145]
	v_mfma_f32_16x16x128_f8f6f4 v[138:141], v[10:17], v[202:209], v[138:141]
	v_mfma_f32_16x16x128_f8f6f4 v[126:129], v[2:9], v[210:217], v[126:129]
	v_mfma_f32_16x16x128_f8f6f4 v[122:125], v[10:17], v[210:217], v[122:125]
	v_mfma_f32_16x16x128_f8f6f4 v[110:113], v[2:9], v[218:225], v[110:113]
	v_mfma_f32_16x16x128_f8f6f4 v[106:109], v[10:17], v[218:225], v[106:109]
	s_setprio 0
	s_setprio 1
	v_mfma_f32_16x16x128_f8f6f4 v[150:153], v[18:25], v[194:201], v[150:153]
	v_mfma_f32_16x16x128_f8f6f4 v[146:149], v[26:33], v[194:201], v[146:149]
	v_mfma_f32_16x16x128_f8f6f4 v[134:137], v[18:25], v[202:209], v[134:137]
	v_mfma_f32_16x16x128_f8f6f4 v[130:133], v[26:33], v[202:209], v[130:133]
	v_mfma_f32_16x16x128_f8f6f4 v[118:121], v[18:25], v[210:217], v[118:121]
	v_mfma_f32_16x16x128_f8f6f4 v[114:117], v[26:33], v[210:217], v[114:117]
	v_mfma_f32_16x16x128_f8f6f4 v[102:105], v[18:25], v[218:225], v[102:105]
	v_mfma_f32_16x16x128_f8f6f4 v[98:101], v[26:33], v[218:225], v[98:101]
	s_setprio 0
	s_barrier
	s_add_i32 s42, s62, s47
	v_lshl_add_u64 v[180:181], v[180:181], 0, s[14:15]
	s_mov_b32 m0, s42
	ds_read_b128 v[194:197], v192 offset:49152
	ds_read_b128 v[198:201], v192 offset:50176
	ds_read_b128 v[202:205], v192 offset:51200
	ds_read_b128 v[206:209], v192 offset:52224
	ds_read_b128 v[210:213], v192 offset:53248
	ds_read_b128 v[214:217], v192 offset:54272
	ds_read_b128 v[218:221], v192 offset:55296
	ds_read_b128 v[222:225], v192 offset:56320
	global_load_lds_dwordx4 v[180:181], off
	s_add_i32 m0, s42, 0x2000
	s_add_u32 s40, s40, 0x40080
	v_lshl_add_u64 v[180:181], v[182:183], 0, s[14:15]
	s_addc_u32 s41, s41, 0
	s_add_i32 s42, s63, s47
	global_load_lds_dwordx4 v[180:181], off
	v_lshl_add_u64 v[180:181], s[40:41], 0, v[166:167]
	s_mov_b32 m0, s42
	s_nop 0
	global_load_lds_dwordx4 v[180:181], off
	v_lshl_add_u64 v[180:181], s[40:41], 0, v[172:173]
	s_add_i32 m0, s42, 0x2000
	s_nop 0
	global_load_lds_dwordx4 v[180:181], off
	v_lshl_add_u64 v[180:181], v[184:185], 0, s[14:15]
	s_mov_b32 m0, s52
	s_nop 0
	global_load_lds_dwordx4 v[180:181], off
	v_lshl_add_u64 v[180:181], v[186:187], 0, s[14:15]
	s_mov_b32 m0, s53
	s_nop 0
	global_load_lds_dwordx4 v[180:181], off
	s_waitcnt vmcnt(8)
	s_waitcnt lgkmcnt(0)
	s_barrier
	s_setprio 1
	s_waitcnt lgkmcnt(0)
	v_mfma_f32_16x16x128_f8f6f4 v[94:97], v[2:9], v[194:201], v[94:97]
	v_mfma_f32_16x16x128_f8f6f4 v[90:93], v[10:17], v[194:201], v[90:93]
	v_mfma_f32_16x16x128_f8f6f4 v[78:81], v[2:9], v[202:209], v[78:81]
	v_mfma_f32_16x16x128_f8f6f4 v[74:77], v[10:17], v[202:209], v[74:77]
	v_mfma_f32_16x16x128_f8f6f4 v[62:65], v[2:9], v[210:217], v[62:65]
	v_mfma_f32_16x16x128_f8f6f4 v[58:61], v[10:17], v[210:217], v[58:61]
	v_mfma_f32_16x16x128_f8f6f4 v[46:49], v[2:9], v[218:225], v[46:49]
	v_mfma_f32_16x16x128_f8f6f4 v[42:45], v[10:17], v[218:225], v[42:45]
	s_setprio 0
	s_setprio 1
	v_mfma_f32_16x16x128_f8f6f4 v[86:89], v[18:25], v[194:201], v[86:89]
	v_mfma_f32_16x16x128_f8f6f4 v[82:85], v[26:33], v[194:201], v[82:85]
	v_mfma_f32_16x16x128_f8f6f4 v[70:73], v[18:25], v[202:209], v[70:73]
	v_mfma_f32_16x16x128_f8f6f4 v[66:69], v[26:33], v[202:209], v[66:69]
	v_mfma_f32_16x16x128_f8f6f4 v[54:57], v[18:25], v[210:217], v[54:57]
	v_mfma_f32_16x16x128_f8f6f4 v[50:53], v[26:33], v[210:217], v[50:53]
	v_mfma_f32_16x16x128_f8f6f4 v[38:41], v[18:25], v[218:225], v[38:41]
	v_mfma_f32_16x16x128_f8f6f4 v[34:37], v[26:33], v[218:225], v[34:37]
	s_setprio 0
	s_barrier
	s_add_i32 s61, s61, 2
	s_add_u32 s6, s6, 0x100
	s_addc_u32 s7, s7, 0
	s_add_u32 s27, s27, 0x100
	s_addc_u32 s39, s39, 0
	s_cmp_gt_u32 s61, 13
	s_cbranch_scc0 .LBB0_1521
	s_nop 15
	s_nop 15
	s_and_b64 vcc, exec, s[16:17]
	s_cbranch_vccz .LBB0_1524
	s_barrier
